# speedup vs baseline: 1.0018x; 1.0018x over previous
_Z16bilateral_kernelPKfS0_Pf:
	s_load_dwordx2 s[4:5], s[0:1], 0x0
	s_load_dwordx2 s[8:9], s[0:1], 0x10
	s_lshr_b32 s19, s2, 8
	s_and_b32 s0, s2, 7
	s_mulk_i32 s0, 0x60
	s_lshr_b32 s1, s2, 3
	s_add_i32 s1, s0, s1
	s_lshr_b32 s0, s1, 6
	s_and_b32 s11, s1, 1
	s_lshl_b32 s11, s11, 8
	s_lshl_b32 s1, s1, 3
	s_nop 0
	s_and_b32 s10, s1, 0x1f0
	s_mov_b32 s1, 0
	s_lshl_b64 s[2:3], s[0:1], 20
	s_mov_b32 s20, 0xc05dfbe6
	s_mov_b32 s21, 0xc05dfbe6
	s_mov_b32 s22, 0xc0a8390e
	s_mov_b32 s23, 0xc0a8390e
	s_mov_b32 s24, 0xc08211a7
	s_mov_b32 s25, 0xc08211a7
	s_mov_b32 s26, 0xc0bb4cc1
	s_mov_b32 s27, 0xc0bb4cc1
	s_mov_b32 s28, 0xc0f487dc
	s_mov_b32 s29, 0xc0f487dc
	s_mov_b32 s30, 0x3e0bd796
	s_mov_b32 s31, 0x3e0bd796
	s_mov_b32 s32, 0x3f45a90c
	s_mov_b32 s33, 0x3f45a90c
	s_mov_b32 s34, 0x3fa5c782
	s_mov_b32 s35, 0x3fa5c782
	v_and_b32_e32 v118, 15, v0
	v_lshrrev_b32_e32 v115, 2, v0
	v_lshl_or_b32 v113, v118, 2, s11
	v_lshrrev_b32_e64 v116, 6, v0
	v_lshl_or_b32 v113, v116, 6, v113
	v_and_or_b32 v117, v115, 12, s10
	v_min_u32_e32 v116, 0x1fa, v113
	v_sub_u32_e64 v115, v113, 2 clamp
	v_add_u32_e64 v116, 4, v116
	v_cmp_eq_u32_e64 s[16:17], 0, v118
	v_cmp_eq_u32_e32 vcc, 15, v118
	s_nop 1
	v_cndmask_b32_e64 v115, v116, v115, s[16:17]
	s_or_b64 vcc, s[16:17], vcc
	v_lshlrev_b32_e32 v115, 2, v115
	v_mov_b32_e32 v116, 0x7ff00000
	s_nop 0
	v_cndmask_b32_e32 v112, v116, v115, vcc
	s_movk_i32 s18, 0x1fc
	v_cmp_eq_u32_e32 vcc, 0, v113
	v_cmp_eq_u32_e64 s[16:17], s18, v113
	v_lshlrev_b32_e32 v113, 2, v113
	s_waitcnt lgkmcnt(0)
	s_add_u32 s4, s4, s2
	s_addc_u32 s5, s5, s3
	s_and_b32 s5, s5, 0xffff
	s_mov_b32 s6, 0x100000
	s_mov_b32 s7, 0x20000
	s_add_u32 s12, s8, s2
	s_addc_u32 s13, s9, s3
	s_and_b32 s13, s13, 0xffff
	s_mov_b32 s14, 0x100000
	s_mov_b32 s15, 0x20000
	v_sub_u32_e64 v115, v117, 2 clamp
	v_lshlrev_b32_e32 v115, 11, v115
	v_add_u32_e32 v116, v115, v112
	v_add_u32_e64 v115, v115, v113
	buffer_load_dwordx2 v[0:1], v116, s[4:7], 0 offen nt
	buffer_load_dwordx2 v[6:7], v116, s[4:7], 0 offen nt
	buffer_load_dwordx4 v[2:5], v115, s[4:7], 0 offen nt
	v_sub_u32_e64 v115, v117, 1 clamp
	v_lshlrev_b32_e32 v115, 11, v115
	v_add_u32_e32 v116, v115, v112
	v_add_u32_e64 v115, v115, v113
	buffer_load_dwordx2 v[8:9], v116, s[4:7], 0 offen nt
	buffer_load_dwordx2 v[14:15], v116, s[4:7], 0 offen nt
	buffer_load_dwordx4 v[10:13], v115, s[4:7], 0 offen nt
	v_lshlrev_b32_e32 v115, 11, v117
	v_add_u32_e32 v116, v115, v112
	v_add_u32_e64 v114, v115, v113
	v_add_u32_e32 v119, 0x1000, v114
	buffer_load_dwordx2 v[16:17], v116, s[4:7], 0 offen nt
	buffer_load_dwordx2 v[22:23], v116, s[4:7], 0 offen nt
	buffer_load_dwordx4 v[18:21], v114, s[4:7], 0 offen nt
	v_lshlrev_b32_e64 v115, 11, v117
	v_add_u32_e32 v115, 0x800, v115
	v_add_u32_e32 v116, v115, v112
	v_add_u32_e32 v115, v115, v113
	buffer_load_dwordx2 v[24:25], v116, s[4:7], 0 offen nt
	buffer_load_dwordx2 v[30:31], v116, s[4:7], 0 offen nt
	buffer_load_dwordx4 v[26:29], v115, s[4:7], 0 offen nt
	v_lshlrev_b32_e64 v115, 11, v117
	v_add_u32_e32 v115, 0x1000, v115
	v_add_u32_e32 v116, v115, v112
	v_add_u32_e32 v115, v115, v113
	buffer_load_dwordx2 v[32:33], v116, s[4:7], 0 offen nt
	buffer_load_dwordx2 v[38:39], v116, s[4:7], 0 offen nt
	buffer_load_dwordx4 v[34:37], v115, s[4:7], 0 offen nt
	v_lshlrev_b32_e64 v115, 11, v117
	v_add_u32_e32 v115, 0x1800, v115
	v_add_u32_e32 v116, v115, v112
	v_add_u32_e32 v115, v115, v113
	buffer_load_dwordx2 v[40:41], v116, s[4:7], 0 offen nt
	buffer_load_dwordx2 v[46:47], v116, s[4:7], 0 offen nt
	buffer_load_dwordx4 v[42:45], v115, s[4:7], 0 offen nt
	v_min_u32_e32 v115, 0x1fb, v117
	v_lshlrev_b32_e64 v115, 11, v115
	v_add_u32_e32 v115, 0x2000, v115
	v_add_u32_e32 v116, v115, v112
	v_add_u32_e32 v115, v115, v113
	buffer_load_dwordx2 v[48:49], v116, s[4:7], 0 offen nt
	buffer_load_dwordx2 v[54:55], v116, s[4:7], 0 offen nt
	buffer_load_dwordx4 v[50:53], v115, s[4:7], 0 offen nt
	v_min_u32_e32 v115, 0x1fa, v117
	v_lshlrev_b32_e64 v115, 11, v115
	v_add_u32_e32 v115, 0x2800, v115
	v_add_u32_e32 v116, v115, v112
	v_add_u32_e32 v115, v115, v113
	buffer_load_dwordx2 v[56:57], v116, s[4:7], 0 offen nt
	buffer_load_dwordx2 v[62:63], v116, s[4:7], 0 offen nt
	buffer_load_dwordx4 v[58:61], v115, s[4:7], 0 offen nt
	s_cmp_eq_u32 s19, 0
	s_cbranch_scc1 .Lmyp0
	s_cmp_eq_u32 s19, 1
	s_cbranch_scc1 .Lmyp1
	s_setprio 0
	s_branch .Lmypd
